# distance-bias look-ups: address = base + 32 t - 32 max(idx, t-113): two VALU per score instead of three (on top of v54)
# speedup vs baseline: 1.0036x; 1.0036x over previous
.LBB0_1332:
	s_and_b64 vcc, exec, s[8:9]
	s_cbranch_vccz .LBB0_1334
	s_sub_i32 s11, s97, 0x71
	s_lshl_b32 s12, s97, 5
	v_add_u32_e32 v252, s12, v140
	s_mov_b32 s12, 0xffffffe0
	s_waitcnt lgkmcnt(7)
	v_max_u32_sdwa v118, s11, v110 dst_sel:DWORD dst_unused:UNUSED_PAD src0_sel:DWORD src1_sel:WORD_0
	v_max_u32_sdwa v110, s11, v110 dst_sel:DWORD dst_unused:UNUSED_PAD src0_sel:DWORD src1_sel:WORD_1
	v_mad_i32_i24 v119, v110, s12, v252
	v_max_u32_sdwa v110, s11, v111 dst_sel:DWORD dst_unused:UNUSED_PAD src0_sel:DWORD src1_sel:WORD_0
	v_mad_i32_i24 v120, v110, s12, v252
	v_max_u32_sdwa v110, s11, v111 dst_sel:DWORD dst_unused:UNUSED_PAD src0_sel:DWORD src1_sel:WORD_1
	v_mad_i32_i24 v121, v110, s12, v252
	v_max_u32_sdwa v110, s11, v112 dst_sel:DWORD dst_unused:UNUSED_PAD src0_sel:DWORD src1_sel:WORD_0
	v_mad_i32_i24 v122, v110, s12, v252
	v_max_u32_sdwa v110, s11, v112 dst_sel:DWORD dst_unused:UNUSED_PAD src0_sel:DWORD src1_sel:WORD_1
	v_mad_i32_i24 v123, v110, s12, v252
	v_max_u32_sdwa v110, s11, v113 dst_sel:DWORD dst_unused:UNUSED_PAD src0_sel:DWORD src1_sel:WORD_0
	v_mad_i32_i24 v124, v110, s12, v252
	v_max_u32_sdwa v110, s11, v113 dst_sel:DWORD dst_unused:UNUSED_PAD src0_sel:DWORD src1_sel:WORD_1
	v_mad_i32_i24 v118, v118, s12, v252
	v_mad_i32_i24 v125, v110, s12, v252
	ds_read_b32 v110, v118
	ds_read_b32 v111, v119
	ds_read_b32 v112, v120
	ds_read_b32 v113, v121
	ds_read_b32 v122, v122
	ds_read_b32 v123, v123
	ds_read_b32 v124, v124
	ds_read_b32 v125, v125
	s_waitcnt lgkmcnt(14)
	v_max_u32_sdwa v118, s11, v106 dst_sel:DWORD dst_unused:UNUSED_PAD src0_sel:DWORD src1_sel:WORD_0
	v_max_u32_sdwa v106, s11, v106 dst_sel:DWORD dst_unused:UNUSED_PAD src0_sel:DWORD src1_sel:WORD_1
	v_mad_i32_i24 v119, v106, s12, v252
	v_max_u32_sdwa v106, s11, v107 dst_sel:DWORD dst_unused:UNUSED_PAD src0_sel:DWORD src1_sel:WORD_0
	v_mad_i32_i24 v120, v106, s12, v252
	v_max_u32_sdwa v106, s11, v107 dst_sel:DWORD dst_unused:UNUSED_PAD src0_sel:DWORD src1_sel:WORD_1
	v_mad_i32_i24 v121, v106, s12, v252
	v_max_u32_sdwa v106, s11, v108 dst_sel:DWORD dst_unused:UNUSED_PAD src0_sel:DWORD src1_sel:WORD_0
	v_mad_i32_i24 v126, v106, s12, v252
	v_max_u32_sdwa v106, s11, v108 dst_sel:DWORD dst_unused:UNUSED_PAD src0_sel:DWORD src1_sel:WORD_1
	v_mad_i32_i24 v127, v106, s12, v252
	v_max_u32_sdwa v106, s11, v109 dst_sel:DWORD dst_unused:UNUSED_PAD src0_sel:DWORD src1_sel:WORD_0
	v_mad_i32_i24 v128, v106, s12, v252
	v_max_u32_sdwa v106, s11, v109 dst_sel:DWORD dst_unused:UNUSED_PAD src0_sel:DWORD src1_sel:WORD_1
	v_mad_i32_i24 v118, v118, s12, v252
	v_mad_i32_i24 v129, v106, s12, v252
	ds_read_b32 v106, v118
	ds_read_b32 v107, v119
	ds_read_b32 v108, v120
	ds_read_b32 v109, v121
	ds_read_b32 v130, v126
	ds_read_b32 v131, v127
	ds_read_b32 v132, v128
	ds_read_b32 v133, v129
	s_waitcnt lgkmcnt(14)
	v_max_u32_sdwa v118, s11, v102 dst_sel:DWORD dst_unused:UNUSED_PAD src0_sel:DWORD src1_sel:WORD_0
	v_max_u32_sdwa v102, s11, v102 dst_sel:DWORD dst_unused:UNUSED_PAD src0_sel:DWORD src1_sel:WORD_1
	v_mad_i32_i24 v119, v102, s12, v252
	v_max_u32_sdwa v102, s11, v103 dst_sel:DWORD dst_unused:UNUSED_PAD src0_sel:DWORD src1_sel:WORD_0
	v_mad_i32_i24 v120, v102, s12, v252
	v_max_u32_sdwa v102, s11, v103 dst_sel:DWORD dst_unused:UNUSED_PAD src0_sel:DWORD src1_sel:WORD_1
	v_mad_i32_i24 v121, v102, s12, v252
	v_max_u32_sdwa v102, s11, v104 dst_sel:DWORD dst_unused:UNUSED_PAD src0_sel:DWORD src1_sel:WORD_0
	v_mad_i32_i24 v126, v102, s12, v252
	v_max_u32_sdwa v102, s11, v104 dst_sel:DWORD dst_unused:UNUSED_PAD src0_sel:DWORD src1_sel:WORD_1
	v_mad_i32_i24 v127, v102, s12, v252
	v_max_u32_sdwa v102, s11, v105 dst_sel:DWORD dst_unused:UNUSED_PAD src0_sel:DWORD src1_sel:WORD_0
	v_mad_i32_i24 v128, v102, s12, v252
	v_max_u32_sdwa v102, s11, v105 dst_sel:DWORD dst_unused:UNUSED_PAD src0_sel:DWORD src1_sel:WORD_1
	v_mad_i32_i24 v118, v118, s12, v252
	v_mad_i32_i24 v129, v102, s12, v252
	ds_read_b32 v102, v118
	ds_read_b32 v103, v119
	ds_read_b32 v104, v120
	ds_read_b32 v105, v121
	ds_read_b32 v156, v126
	ds_read_b32 v157, v127
	ds_read_b32 v158, v128
	ds_read_b32 v159, v129
	v_max_u32_sdwa v118, s11, v98 dst_sel:DWORD dst_unused:UNUSED_PAD src0_sel:DWORD src1_sel:WORD_0
	v_max_u32_sdwa v98, s11, v98 dst_sel:DWORD dst_unused:UNUSED_PAD src0_sel:DWORD src1_sel:WORD_1
	v_mad_i32_i24 v119, v98, s12, v252
	v_max_u32_sdwa v98, s11, v99 dst_sel:DWORD dst_unused:UNUSED_PAD src0_sel:DWORD src1_sel:WORD_0
	v_mad_i32_i24 v120, v98, s12, v252
	v_max_u32_sdwa v98, s11, v99 dst_sel:DWORD dst_unused:UNUSED_PAD src0_sel:DWORD src1_sel:WORD_1
	v_mad_i32_i24 v121, v98, s12, v252
	v_max_u32_sdwa v98, s11, v100 dst_sel:DWORD dst_unused:UNUSED_PAD src0_sel:DWORD src1_sel:WORD_0
	v_mad_i32_i24 v126, v98, s12, v252
	v_max_u32_sdwa v98, s11, v100 dst_sel:DWORD dst_unused:UNUSED_PAD src0_sel:DWORD src1_sel:WORD_1
	v_mad_i32_i24 v127, v98, s12, v252
	v_max_u32_sdwa v98, s11, v101 dst_sel:DWORD dst_unused:UNUSED_PAD src0_sel:DWORD src1_sel:WORD_0
	v_mad_i32_i24 v128, v98, s12, v252
	v_max_u32_sdwa v98, s11, v101 dst_sel:DWORD dst_unused:UNUSED_PAD src0_sel:DWORD src1_sel:WORD_1
	v_mad_i32_i24 v118, v118, s12, v252
	v_mad_i32_i24 v129, v98, s12, v252
	ds_read_b32 v98, v118
	ds_read_b32 v99, v119
	ds_read_b32 v100, v120
	ds_read_b32 v101, v121
	ds_read_b32 v164, v126
	ds_read_b32 v165, v127
	ds_read_b32 v166, v128
	ds_read_b32 v167, v129
	v_pk_fma_f32 v[118:119], v[30:31], s[54:55], v[110:111] op_sel_hi:[1,0,1]
	s_waitcnt lgkmcnt(14)
	v_pk_fma_f32 v[120:121], v[32:33], s[54:55], v[112:113] op_sel_hi:[1,0,1]
	v_max3_f32 v30, v118, s23, v119
	v_max3_f32 v30, v30, v120, v121
	v_pk_fma_f32 v[122:123], v[42:43], s[54:55], v[122:123] op_sel_hi:[1,0,1]
	v_pk_fma_f32 v[124:125], v[44:45], s[54:55], v[124:125] op_sel_hi:[1,0,1]
	v_max3_f32 v30, v30, v122, v123
	v_max3_f32 v30, v30, v124, v125
	v_pk_fma_f32 v[126:127], v[46:47], s[54:55], v[106:107] op_sel_hi:[1,0,1]
	v_pk_fma_f32 v[128:129], v[48:49], s[54:55], v[108:109] op_sel_hi:[1,0,1]
	v_max3_f32 v30, v30, v126, v127
	v_max3_f32 v30, v30, v128, v129
	v_pk_fma_f32 v[130:131], v[50:51], s[54:55], v[130:131] op_sel_hi:[1,0,1]
	v_pk_fma_f32 v[132:133], v[52:53], s[54:55], v[132:133] op_sel_hi:[1,0,1]
	v_max3_f32 v30, v30, v130, v131
	v_max3_f32 v30, v30, v132, v133
	v_pk_fma_f32 v[134:135], v[58:59], s[54:55], v[102:103] op_sel_hi:[1,0,1]
	s_waitcnt lgkmcnt(12)
	v_pk_fma_f32 v[136:137], v[60:61], s[54:55], v[104:105] op_sel_hi:[1,0,1]
	v_max3_f32 v30, v30, v134, v135
	v_max3_f32 v30, v30, v136, v137
	s_waitcnt lgkmcnt(10)
	v_pk_fma_f32 v[156:157], v[62:63], s[54:55], v[156:157] op_sel_hi:[1,0,1]
	s_waitcnt lgkmcnt(8)
	v_pk_fma_f32 v[158:159], v[64:65], s[54:55], v[158:159] op_sel_hi:[1,0,1]
	v_max3_f32 v30, v30, v156, v157
	v_max3_f32 v30, v30, v158, v159
	s_waitcnt lgkmcnt(6)
	v_pk_fma_f32 v[160:161], v[70:71], s[54:55], v[98:99] op_sel_hi:[1,0,1]
	s_waitcnt lgkmcnt(4)
	v_pk_fma_f32 v[162:163], v[72:73], s[54:55], v[100:101] op_sel_hi:[1,0,1]
	v_max3_f32 v30, v30, v160, v161
	v_max3_f32 v30, v30, v162, v163
	s_waitcnt lgkmcnt(2)
	v_pk_fma_f32 v[164:165], v[78:79], s[54:55], v[164:165] op_sel_hi:[1,0,1]
	s_waitcnt lgkmcnt(0)
	v_pk_fma_f32 v[166:167], v[80:81], s[54:55], v[166:167] op_sel_hi:[1,0,1]
	v_max3_f32 v30, v30, v164, v165
	v_max3_f32 v98, v30, v166, v167
	v_max_u32_sdwa v30, s11, v94 dst_sel:DWORD dst_unused:UNUSED_PAD src0_sel:DWORD src1_sel:WORD_0
	v_max_u32_sdwa v31, s11, v94 dst_sel:DWORD dst_unused:UNUSED_PAD src0_sel:DWORD src1_sel:WORD_1
	v_max_u32_sdwa v32, s11, v95 dst_sel:DWORD dst_unused:UNUSED_PAD src0_sel:DWORD src1_sel:WORD_0
	v_max_u32_sdwa v33, s11, v95 dst_sel:DWORD dst_unused:UNUSED_PAD src0_sel:DWORD src1_sel:WORD_1
	v_max_u32_sdwa v42, s11, v96 dst_sel:DWORD dst_unused:UNUSED_PAD src0_sel:DWORD src1_sel:WORD_0
	v_max_u32_sdwa v43, s11, v96 dst_sel:DWORD dst_unused:UNUSED_PAD src0_sel:DWORD src1_sel:WORD_1
	v_max_u32_sdwa v44, s11, v97 dst_sel:DWORD dst_unused:UNUSED_PAD src0_sel:DWORD src1_sel:WORD_0
	v_max_u32_sdwa v45, s11, v97 dst_sel:DWORD dst_unused:UNUSED_PAD src0_sel:DWORD src1_sel:WORD_1
	s_waitcnt lgkmcnt(0)
	v_mad_i32_i24 v30, v30, s12, v252
	v_mad_i32_i24 v31, v31, s12, v252
	v_mad_i32_i24 v32, v32, s12, v252
	v_mad_i32_i24 v33, v33, s12, v252
	v_mad_i32_i24 v42, v42, s12, v252
	v_mad_i32_i24 v43, v43, s12, v252
	v_mad_i32_i24 v44, v44, s12, v252
	v_mad_i32_i24 v45, v45, s12, v252
	ds_read_b32 v30, v30
	ds_read_b32 v31, v31
	ds_read_b32 v32, v32
	ds_read_b32 v33, v33
	ds_read_b32 v42, v42
	ds_read_b32 v43, v43
	ds_read_b32 v44, v44
	ds_read_b32 v45, v45
	v_max_u32_sdwa v46, s11, v90 dst_sel:DWORD dst_unused:UNUSED_PAD src0_sel:DWORD src1_sel:WORD_0
	v_max_u32_sdwa v47, s11, v90 dst_sel:DWORD dst_unused:UNUSED_PAD src0_sel:DWORD src1_sel:WORD_1
	v_max_u32_sdwa v48, s11, v91 dst_sel:DWORD dst_unused:UNUSED_PAD src0_sel:DWORD src1_sel:WORD_0
	v_max_u32_sdwa v49, s11, v91 dst_sel:DWORD dst_unused:UNUSED_PAD src0_sel:DWORD src1_sel:WORD_1
	v_max_u32_sdwa v50, s11, v92 dst_sel:DWORD dst_unused:UNUSED_PAD src0_sel:DWORD src1_sel:WORD_0
	v_max_u32_sdwa v51, s11, v92 dst_sel:DWORD dst_unused:UNUSED_PAD src0_sel:DWORD src1_sel:WORD_1
	v_max_u32_sdwa v52, s11, v93 dst_sel:DWORD dst_unused:UNUSED_PAD src0_sel:DWORD src1_sel:WORD_0
	v_max_u32_sdwa v53, s11, v93 dst_sel:DWORD dst_unused:UNUSED_PAD src0_sel:DWORD src1_sel:WORD_1
	s_waitcnt lgkmcnt(6)
	v_pk_fma_f32 v[168:169], v[18:19], s[54:55], v[30:31] op_sel_hi:[1,0,1]
	v_mad_i32_i24 v46, v46, s12, v252
	v_mad_i32_i24 v47, v47, s12, v252
	v_mad_i32_i24 v48, v48, s12, v252
	v_mad_i32_i24 v49, v49, s12, v252
	v_mad_i32_i24 v50, v50, s12, v252
	v_mad_i32_i24 v51, v51, s12, v252
	v_mad_i32_i24 v52, v52, s12, v252
	v_mad_i32_i24 v53, v53, s12, v252
	v_max3_f32 v18, v98, v168, v169
	s_waitcnt lgkmcnt(4)
	v_pk_fma_f32 v[170:171], v[20:21], s[54:55], v[32:33] op_sel_hi:[1,0,1]
	ds_read_b32 v46, v46
	ds_read_b32 v47, v47
	ds_read_b32 v48, v48
	ds_read_b32 v49, v49
	ds_read_b32 v50, v50
	ds_read_b32 v51, v51
	ds_read_b32 v52, v52
	ds_read_b32 v53, v53
	v_max3_f32 v18, v18, v170, v171
	s_waitcnt lgkmcnt(10)
	v_pk_fma_f32 v[172:173], v[22:23], s[54:55], v[42:43] op_sel_hi:[1,0,1]
	v_max_u32_sdwa v58, s11, v86 dst_sel:DWORD dst_unused:UNUSED_PAD src0_sel:DWORD src1_sel:WORD_0
	v_max_u32_sdwa v59, s11, v86 dst_sel:DWORD dst_unused:UNUSED_PAD src0_sel:DWORD src1_sel:WORD_1
	v_max_u32_sdwa v60, s11, v87 dst_sel:DWORD dst_unused:UNUSED_PAD src0_sel:DWORD src1_sel:WORD_0
	v_max_u32_sdwa v61, s11, v87 dst_sel:DWORD dst_unused:UNUSED_PAD src0_sel:DWORD src1_sel:WORD_1
	v_max_u32_sdwa v62, s11, v88 dst_sel:DWORD dst_unused:UNUSED_PAD src0_sel:DWORD src1_sel:WORD_0
	v_max_u32_sdwa v63, s11, v88 dst_sel:DWORD dst_unused:UNUSED_PAD src0_sel:DWORD src1_sel:WORD_1
	v_max_u32_sdwa v64, s11, v89 dst_sel:DWORD dst_unused:UNUSED_PAD src0_sel:DWORD src1_sel:WORD_0
	v_max_u32_sdwa v65, s11, v89 dst_sel:DWORD dst_unused:UNUSED_PAD src0_sel:DWORD src1_sel:WORD_1
	v_max3_f32 v18, v18, v172, v173
	s_waitcnt lgkmcnt(8)
	v_pk_fma_f32 v[174:175], v[24:25], s[54:55], v[44:45] op_sel_hi:[1,0,1]
	v_max3_f32 v18, v18, v174, v175
	s_waitcnt lgkmcnt(6)
	v_pk_fma_f32 v[176:177], v[26:27], s[54:55], v[46:47] op_sel_hi:[1,0,1]
	v_mad_i32_i24 v58, v58, s12, v252
	v_mad_i32_i24 v59, v59, s12, v252
	v_mad_i32_i24 v60, v60, s12, v252
	v_mad_i32_i24 v61, v61, s12, v252
	v_mad_i32_i24 v62, v62, s12, v252
	v_mad_i32_i24 v63, v63, s12, v252
	v_mad_i32_i24 v64, v64, s12, v252
	v_mad_i32_i24 v65, v65, s12, v252
	v_max3_f32 v18, v18, v176, v177
	s_waitcnt lgkmcnt(4)
	v_pk_fma_f32 v[178:179], v[28:29], s[54:55], v[48:49] op_sel_hi:[1,0,1]
	ds_read_b32 v58, v58
	ds_read_b32 v59, v59
	ds_read_b32 v60, v60
	ds_read_b32 v61, v61
	ds_read_b32 v62, v62
	ds_read_b32 v63, v63
	ds_read_b32 v64, v64
	ds_read_b32 v65, v65
	v_max3_f32 v18, v18, v178, v179
	s_waitcnt lgkmcnt(10)
	v_pk_fma_f32 v[180:181], v[34:35], s[54:55], v[50:51] op_sel_hi:[1,0,1]
	v_max_u32_sdwa v70, s11, v82 dst_sel:DWORD dst_unused:UNUSED_PAD src0_sel:DWORD src1_sel:WORD_0
	v_max_u32_sdwa v71, s11, v82 dst_sel:DWORD dst_unused:UNUSED_PAD src0_sel:DWORD src1_sel:WORD_1
	v_max_u32_sdwa v72, s11, v83 dst_sel:DWORD dst_unused:UNUSED_PAD src0_sel:DWORD src1_sel:WORD_0
	v_max_u32_sdwa v73, s11, v83 dst_sel:DWORD dst_unused:UNUSED_PAD src0_sel:DWORD src1_sel:WORD_1
	v_max_u32_sdwa v78, s11, v84 dst_sel:DWORD dst_unused:UNUSED_PAD src0_sel:DWORD src1_sel:WORD_0
	v_max_u32_sdwa v79, s11, v84 dst_sel:DWORD dst_unused:UNUSED_PAD src0_sel:DWORD src1_sel:WORD_1
	v_max_u32_sdwa v80, s11, v85 dst_sel:DWORD dst_unused:UNUSED_PAD src0_sel:DWORD src1_sel:WORD_0
	v_max_u32_sdwa v81, s11, v85 dst_sel:DWORD dst_unused:UNUSED_PAD src0_sel:DWORD src1_sel:WORD_1
	v_max3_f32 v18, v18, v180, v181
	s_waitcnt lgkmcnt(8)
	v_pk_fma_f32 v[182:183], v[36:37], s[54:55], v[52:53] op_sel_hi:[1,0,1]
	v_max3_f32 v18, v18, v182, v183
	s_waitcnt lgkmcnt(6)
	v_pk_fma_f32 v[184:185], v[38:39], s[54:55], v[58:59] op_sel_hi:[1,0,1]
	v_mad_i32_i24 v70, v70, s12, v252
	v_mad_i32_i24 v71, v71, s12, v252
	v_mad_i32_i24 v72, v72, s12, v252
	v_mad_i32_i24 v73, v73, s12, v252
	v_mad_i32_i24 v78, v78, s12, v252
	v_mad_i32_i24 v79, v79, s12, v252
	v_mad_i32_i24 v80, v80, s12, v252
	v_mad_i32_i24 v81, v81, s12, v252
	v_max3_f32 v18, v18, v184, v185
	s_waitcnt lgkmcnt(4)
	v_pk_fma_f32 v[186:187], v[40:41], s[54:55], v[60:61] op_sel_hi:[1,0,1]
	ds_read_b32 v70, v70
	ds_read_b32 v71, v71
	ds_read_b32 v72, v72
	ds_read_b32 v73, v73
	ds_read_b32 v78, v78
	ds_read_b32 v79, v79
	ds_read_b32 v80, v80
	ds_read_b32 v81, v81
	v_max3_f32 v18, v18, v186, v187
	s_waitcnt lgkmcnt(10)
	v_pk_fma_f32 v[188:189], v[54:55], s[54:55], v[62:63] op_sel_hi:[1,0,1]
	s_waitcnt lgkmcnt(8)
	v_pk_fma_f32 v[190:191], v[56:57], s[54:55], v[64:65] op_sel_hi:[1,0,1]
	v_max3_f32 v18, v18, v188, v189
	v_max3_f32 v18, v18, v190, v191
	s_waitcnt lgkmcnt(6)
	v_pk_fma_f32 v[192:193], v[66:67], s[54:55], v[70:71] op_sel_hi:[1,0,1]
	s_waitcnt lgkmcnt(0)
	s_waitcnt lgkmcnt(4)
	v_pk_fma_f32 v[194:195], v[68:69], s[54:55], v[72:73] op_sel_hi:[1,0,1]
	v_max3_f32 v18, v18, v192, v193
	v_max3_f32 v18, v18, v194, v195
	s_waitcnt lgkmcnt(2)
	v_pk_fma_f32 v[196:197], v[74:75], s[54:55], v[78:79] op_sel_hi:[1,0,1]
	s_waitcnt lgkmcnt(0)
	v_pk_fma_f32 v[198:199], v[76:77], s[54:55], v[80:81] op_sel_hi:[1,0,1]
	v_max3_f32 v18, v18, v196, v197
	v_max3_f32 v215, v18, v198, v199
